# gcn layer-2 fast path: recompute MFMAs take the bias through their C operand (4 v_mov per column tile instead of 8 v_add)
# speedup vs baseline: 1.0188x; 1.0072x over previous
.LBB5_22:
	s_or_b64 exec, exec, s[14:15]
	v_lshl_or_b32 v74, v74, 6, v109
	global_load_dwordx4 v[74:77], v74, s[10:11]
	s_waitcnt vmcnt(1)
	v_mov_b32_e32 v124, v65
	v_mov_b32_e32 v125, v65
	v_mov_b32_e32 v126, v65
	v_mov_b32_e32 v127, v65
	v_add_u32_e32 v93, -1, v93
	s_add_i32 s29, s29, 32
	s_add_i32 s28, s28, 2
	v_cmp_eq_u32_e32 vcc, 0, v93
	v_add_u32_e32 v106, 0x100, v106
	v_mfma_f32_16x16x32_f16 v[112:115], v[70:73], v[32:35], v[124:127]
	s_waitcnt vmcnt(0)
	v_mfma_f32_16x16x32_f16 v[116:119], v[74:77], v[32:35], v[124:127]
	s_nop 1
	s_or_b64 s[12:13], vcc, s[12:13]
	s_nop 1
	v_mov_b32_e32 v124, v94
	v_mov_b32_e32 v125, v94
	v_mov_b32_e32 v126, v94
	v_mov_b32_e32 v127, v94
	v_cvt_pk_f16_f32 v112, v112, v113
	v_cvt_pk_f16_f32 v113, v114, v115
	v_cvt_pk_f16_f32 v114, v116, v117
	v_cvt_pk_f16_f32 v115, v118, v119
	v_mfma_f32_16x16x32_f16 v[116:119], v[74:77], v[36:39], v[124:127]
	v_mfma_f32_16x16x32_f16 v[120:123], v[70:73], v[36:39], v[124:127]
	v_pk_max_f16 v112, v112, 0
	v_pk_max_f16 v113, v113, 0
	v_pk_max_f16 v114, v114, 0
	v_pk_max_f16 v115, v115, 0
	s_nop 1
	v_mfma_f32_16x16x32_f16 v[28:31], v[112:115], v[66:69], v[28:31]
	v_mov_b32_e32 v124, v95
	v_mov_b32_e32 v125, v95
	v_mov_b32_e32 v126, v95
	v_mov_b32_e32 v127, v95
	v_cvt_pk_f16_f32 v120, v120, v121
	v_cvt_pk_f16_f32 v121, v122, v123
	v_cvt_pk_f16_f32 v122, v116, v117
	v_cvt_pk_f16_f32 v123, v118, v119
	v_mfma_f32_16x16x32_f16 v[116:119], v[74:77], v[40:43], v[124:127]
	v_mfma_f32_16x16x32_f16 v[112:115], v[70:73], v[40:43], v[124:127]
	v_pk_max_f16 v120, v120, 0
	v_pk_max_f16 v121, v121, 0
	v_pk_max_f16 v122, v122, 0
	v_pk_max_f16 v123, v123, 0
	s_nop 1
	v_mfma_f32_16x16x32_f16 v[24:27], v[120:123], v[66:69], v[24:27]
	v_mov_b32_e32 v124, v96
	v_mov_b32_e32 v125, v96
	v_mov_b32_e32 v126, v96
	v_mov_b32_e32 v127, v96
	v_cvt_pk_f16_f32 v112, v112, v113
	v_cvt_pk_f16_f32 v113, v114, v115
	v_cvt_pk_f16_f32 v114, v116, v117
	v_cvt_pk_f16_f32 v115, v118, v119
	v_mfma_f32_16x16x32_f16 v[116:119], v[74:77], v[44:47], v[124:127]
	v_mfma_f32_16x16x32_f16 v[120:123], v[70:73], v[44:47], v[124:127]
	v_pk_max_f16 v112, v112, 0
	v_pk_max_f16 v113, v113, 0
	v_pk_max_f16 v114, v114, 0
	v_pk_max_f16 v115, v115, 0
	s_nop 1
	v_mfma_f32_16x16x32_f16 v[20:23], v[112:115], v[66:69], v[20:23]
	v_mov_b32_e32 v124, v97
	v_mov_b32_e32 v125, v97
	v_mov_b32_e32 v126, v97
	v_mov_b32_e32 v127, v97
	v_cvt_pk_f16_f32 v120, v120, v121
	v_cvt_pk_f16_f32 v121, v122, v123
	v_cvt_pk_f16_f32 v122, v116, v117
	v_cvt_pk_f16_f32 v123, v118, v119
	v_mfma_f32_16x16x32_f16 v[116:119], v[74:77], v[48:51], v[124:127]
	v_mfma_f32_16x16x32_f16 v[112:115], v[70:73], v[48:51], v[124:127]
	v_pk_max_f16 v120, v120, 0
	v_pk_max_f16 v121, v121, 0
	v_pk_max_f16 v122, v122, 0
	v_pk_max_f16 v123, v123, 0
	s_nop 1
	v_mfma_f32_16x16x32_f16 v[16:19], v[120:123], v[66:69], v[16:19]
	v_mov_b32_e32 v124, v98
	v_mov_b32_e32 v125, v98
	v_mov_b32_e32 v126, v98
	v_mov_b32_e32 v127, v98
	v_cvt_pk_f16_f32 v112, v112, v113
	v_cvt_pk_f16_f32 v113, v114, v115
	v_cvt_pk_f16_f32 v114, v116, v117
	v_cvt_pk_f16_f32 v115, v118, v119
	v_mfma_f32_16x16x32_f16 v[116:119], v[74:77], v[52:55], v[124:127]
	v_mfma_f32_16x16x32_f16 v[120:123], v[70:73], v[52:55], v[124:127]
	v_pk_max_f16 v112, v112, 0
	v_pk_max_f16 v113, v113, 0
	v_pk_max_f16 v114, v114, 0
	v_pk_max_f16 v115, v115, 0
	s_nop 1
	v_mfma_f32_16x16x32_f16 v[12:15], v[112:115], v[66:69], v[12:15]
	v_mov_b32_e32 v124, v99
	v_mov_b32_e32 v125, v99
	v_mov_b32_e32 v126, v99
	v_mov_b32_e32 v127, v99
	v_cvt_pk_f16_f32 v120, v120, v121
	v_cvt_pk_f16_f32 v121, v122, v123
	v_cvt_pk_f16_f32 v122, v116, v117
	v_cvt_pk_f16_f32 v123, v118, v119
	v_mfma_f32_16x16x32_f16 v[116:119], v[74:77], v[56:59], v[124:127]
	v_mfma_f32_16x16x32_f16 v[112:115], v[70:73], v[56:59], v[124:127]
	v_pk_max_f16 v120, v120, 0
	v_pk_max_f16 v121, v121, 0
	v_pk_max_f16 v122, v122, 0
	v_pk_max_f16 v123, v123, 0
	s_nop 1
	v_mfma_f32_16x16x32_f16 v[8:11], v[120:123], v[66:69], v[8:11]
	v_mov_b32_e32 v124, v100
	v_mov_b32_e32 v125, v100
	v_mov_b32_e32 v126, v100
	v_mov_b32_e32 v127, v100
	v_cvt_pk_f16_f32 v112, v112, v113
	v_cvt_pk_f16_f32 v113, v114, v115
	v_cvt_pk_f16_f32 v114, v116, v117
	v_cvt_pk_f16_f32 v115, v118, v119
	v_mfma_f32_16x16x32_f16 v[116:119], v[74:77], v[60:63], v[124:127]
	v_mfma_f32_16x16x32_f16 v[120:123], v[70:73], v[60:63], v[124:127]
	v_pk_max_f16 v112, v112, 0
	v_pk_max_f16 v113, v113, 0
	v_pk_max_f16 v114, v114, 0
	v_pk_max_f16 v115, v115, 0
	s_nop 1
	v_mfma_f32_16x16x32_f16 v[4:7], v[112:115], v[66:69], v[4:7]
	s_nop 3
	v_cvt_pk_f16_f32 v120, v120, v121
	v_cvt_pk_f16_f32 v121, v122, v123
	v_cvt_pk_f16_f32 v122, v116, v117
	v_cvt_pk_f16_f32 v123, v118, v119
	v_pk_max_f16 v120, v120, 0
	v_pk_max_f16 v121, v121, 0
	v_pk_max_f16 v122, v122, 0
	v_pk_max_f16 v123, v123, 0
	s_nop 1
	v_mfma_f32_16x16x32_f16 v[0:3], v[120:123], v[66:69], v[0:3]
	s_andn2_b64 exec, exec, s[12:13]
	s_cbranch_execz .LBB5_43

	.amdhsa_kernel _Z5k_gcnILi2EEvPKvPK15HIP_vector_typeIiLj2EEPfPKiS8_PKfPKDF16_SA_SA_SA_SA_S6_PDF16_S6_SD_SC_SA_
		.amdhsa_group_segment_fixed_size 23808
		.amdhsa_private_segment_fixed_size 0
		.amdhsa_kernarg_size 392
		.amdhsa_user_sgpr_count 2
		.amdhsa_user_sgpr_dispatch_ptr 0
		.amdhsa_user_sgpr_queue_ptr 0
		.amdhsa_user_sgpr_kernarg_segment_ptr 1
		.amdhsa_user_sgpr_dispatch_id 0
		.amdhsa_user_sgpr_kernarg_preload_length 0
		.amdhsa_user_sgpr_kernarg_preload_offset 0
		.amdhsa_user_sgpr_private_segment_size 0
		.amdhsa_uses_dynamic_stack 0
		.amdhsa_enable_private_segment 0
		.amdhsa_system_sgpr_workgroup_id_x 1
		.amdhsa_system_sgpr_workgroup_id_y 0
		.amdhsa_system_sgpr_workgroup_id_z 0
		.amdhsa_system_sgpr_workgroup_info 0
		.amdhsa_system_vgpr_workitem_id 2
		.amdhsa_next_free_vgpr 128
		.amdhsa_next_free_sgpr 91
		.amdhsa_accum_offset 128
		.amdhsa_reserve_vcc 1
		.amdhsa_float_round_mode_32 0
		.amdhsa_float_round_mode_16_64 0
		.amdhsa_float_denorm_mode_32 3
		.amdhsa_float_denorm_mode_16_64 3
		.amdhsa_dx10_clamp 1
		.amdhsa_ieee_mode 1
		.amdhsa_fp16_overflow 0
		.amdhsa_tg_split 0
		.amdhsa_exception_fp_ieee_invalid_op 0
		.amdhsa_exception_fp_denorm_src 0
		.amdhsa_exception_fp_ieee_div_zero 0
		.amdhsa_exception_fp_ieee_overflow 0
		.amdhsa_exception_fp_ieee_underflow 0
		.amdhsa_exception_fp_ieee_inexact 0
		.amdhsa_exception_int_div_zero 0
	.end_amdhsa_kernel

amdhsa.kernels:
  - .agpr_count:     0
    .args:
      - .actual_access:  read_only
        .address_space:  global
        .offset:         0
        .size:           8
        .value_kind:     global_buffer
      - .actual_access:  read_only
        .address_space:  global
        .offset:         8
        .size:           8
        .value_kind:     global_buffer
      - .actual_access:  read_only
        .address_space:  global
        .offset:         16
        .size:           8
        .value_kind:     global_buffer
      - .actual_access:  read_only
        .address_space:  global
        .offset:         24
        .size:           8
        .value_kind:     global_buffer
      - .actual_access:  write_only
        .address_space:  global
        .offset:         32
        .size:           8
        .value_kind:     global_buffer
      - .actual_access:  write_only
        .address_space:  global
        .offset:         40
        .size:           8
        .value_kind:     global_buffer
    .group_segment_fixed_size: 56512
    .kernarg_segment_align: 8
    .kernarg_segment_size: 48
    .language:       OpenCL C
    .language_version:
      - 2
      - 0
    .max_flat_workgroup_size: 1024
    .name:           _Z10k_bscatterPKiS0_PKfS0_PiP15HIP_vector_typeIiLj2EE
    .private_segment_fixed_size: 0
    .sgpr_count:     42
    .sgpr_spill_count: 0
    .symbol:         _Z10k_bscatterPKiS0_PKfS0_PiP15HIP_vector_typeIiLj2EE.kd
    .uniform_work_group_size: 1
    .uses_dynamic_stack: false
    .vgpr_count:     89
    .vgpr_spill_count: 0
    .wavefront_size: 64
  - .agpr_count:     0
    .args:
      - .actual_access:  read_only
        .address_space:  global
        .offset:         0
        .size:           8
        .value_kind:     global_buffer
      - .actual_access:  read_only
        .address_space:  global
        .offset:         8
        .size:           8
        .value_kind:     global_buffer
      - .actual_access:  write_only
        .address_space:  global
        .offset:         16
        .size:           8
        .value_kind:     global_buffer
      - .actual_access:  write_only
        .address_space:  global
        .offset:         24
        .size:           8
        .value_kind:     global_buffer
      - .actual_access:  write_only
        .address_space:  global
        .offset:         32
        .size:           8
        .value_kind:     global_buffer
      - .actual_access:  write_only
        .address_space:  global
        .offset:         40
        .size:           8
        .value_kind:     global_buffer
      - .actual_access:  read_only
        .address_space:  global
        .offset:         48
        .size:           8
        .value_kind:     global_buffer
      - .actual_access:  write_only
        .address_space:  global
        .offset:         56
        .size:           8
        .value_kind:     global_buffer
    .group_segment_fixed_size: 12352
    .kernarg_segment_align: 8
    .kernarg_segment_size: 64
    .language:       OpenCL C
    .language_version:
      - 2
      - 0
    .max_flat_workgroup_size: 1024
    .name:           _Z8k_bfinalPK15HIP_vector_typeIiLj2EEPKiPS0_PiS6_PfPKfPDF16_
    .private_segment_fixed_size: 0
    .sgpr_count:     38
    .sgpr_spill_count: 0
    .symbol:         _Z8k_bfinalPK15HIP_vector_typeIiLj2EEPKiPS0_PiS6_PfPKfPDF16_.kd
    .uniform_work_group_size: 1
    .uses_dynamic_stack: false
    .vgpr_count:     72
    .vgpr_spill_count: 0
    .wavefront_size: 64
  - .agpr_count:     0
    .args:
      - .actual_access:  read_only
        .address_space:  global
        .offset:         0
        .size:           8
        .value_kind:     global_buffer
      - .actual_access:  write_only
        .address_space:  global
        .offset:         8
        .size:           8
        .value_kind:     global_buffer
      - .actual_access:  write_only
        .address_space:  global
        .offset:         16
        .size:           8
        .value_kind:     global_buffer
      - .actual_access:  read_only
        .address_space:  global
        .offset:         24
        .size:           8
        .value_kind:     global_buffer
      - .actual_access:  read_only
        .address_space:  global
        .offset:         32
        .size:           8
        .value_kind:     global_buffer
      - .actual_access:  write_only
        .address_space:  global
        .offset:         40
        .size:           8
        .value_kind:     global_buffer
      - .actual_access:  read_only
        .address_space:  global
        .offset:         48
        .size:           8
        .value_kind:     global_buffer
      - .actual_access:  read_only
        .address_space:  global
        .offset:         56
        .size:           8
        .value_kind:     global_buffer
      - .actual_access:  read_only
        .address_space:  global
        .offset:         64
        .size:           8
        .value_kind:     global_buffer
      - .actual_access:  read_only
        .address_space:  global
        .offset:         72
        .size:           8
        .value_kind:     global_buffer
      - .actual_access:  read_only
        .address_space:  global
        .offset:         80
        .size:           8
        .value_kind:     global_buffer
      - .actual_access:  read_only
        .address_space:  global
        .offset:         88
        .size:           8
        .value_kind:     global_buffer
      - .actual_access:  write_only
        .address_space:  global
        .offset:         96
        .size:           8
        .value_kind:     global_buffer
      - .actual_access:  write_only
        .address_space:  global
        .offset:         104
        .size:           8
        .value_kind:     global_buffer
      - .actual_access:  write_only
        .address_space:  global
        .offset:         112
        .size:           8
        .value_kind:     global_buffer
      - .actual_access:  write_only
        .address_space:  global
        .offset:         120
        .size:           8
        .value_kind:     global_buffer
      - .actual_access:  write_only
        .address_space:  global
        .offset:         128
        .size:           8
        .value_kind:     global_buffer
    .group_segment_fixed_size: 628
    .kernarg_segment_align: 8
    .kernarg_segment_size: 136
    .language:       OpenCL C
    .language_version:
      - 2
      - 0
    .max_flat_workgroup_size: 1024
    .name:           _Z7k_bhistPKiPiPfPKfS4_PDF16_S4_S4_S4_S4_S4_S4_S5_S5_S5_S5_S2_
    .private_segment_fixed_size: 0
    .sgpr_count:     25
    .sgpr_spill_count: 0
    .symbol:         _Z7k_bhistPKiPiPfPKfS4_PDF16_S4_S4_S4_S4_S4_S4_S5_S5_S5_S5_S2_.kd
    .uniform_work_group_size: 1
    .uses_dynamic_stack: false
    .vgpr_count:     32
    .vgpr_spill_count: 0
    .wavefront_size: 64
  - .agpr_count:     0
    .args:
      - .actual_access:  read_only
        .address_space:  global
        .offset:         0
        .size:           8
        .value_kind:     global_buffer
      - .actual_access:  read_only
        .address_space:  global
        .offset:         8
        .size:           8
        .value_kind:     global_buffer
      - .actual_access:  read_only
        .address_space:  global
        .offset:         16
        .size:           8
        .value_kind:     global_buffer
      - .actual_access:  read_only
        .address_space:  global
        .offset:         24
        .size:           8
        .value_kind:     global_buffer
      - .actual_access:  read_only
        .address_space:  global
        .offset:         32
        .size:           8
        .value_kind:     global_buffer
      - .actual_access:  read_only
        .address_space:  global
        .offset:         40
        .size:           8
        .value_kind:     global_buffer
      - .actual_access:  read_only
        .address_space:  global
        .offset:         48
        .size:           8
        .value_kind:     global_buffer
      - .actual_access:  read_only
        .address_space:  global
        .offset:         56
        .size:           8
        .value_kind:     global_buffer
      - .actual_access:  read_only
        .address_space:  global
        .offset:         64
        .size:           8
        .value_kind:     global_buffer
      - .actual_access:  write_only
        .address_space:  global
        .offset:         72
        .size:           8
        .value_kind:     global_buffer
      - .actual_access:  write_only
        .address_space:  global
        .offset:         80
        .size:           8
        .value_kind:     global_buffer
      - .offset:         88
        .size:           4
        .value_kind:     hidden_block_count_x
      - .offset:         92
        .size:           4
        .value_kind:     hidden_block_count_y
      - .offset:         96
        .size:           4
        .value_kind:     hidden_block_count_z
      - .offset:         100
        .size:           2
        .value_kind:     hidden_group_size_x
      - .offset:         102
        .size:           2
        .value_kind:     hidden_group_size_y
      - .offset:         104
        .size:           2
        .value_kind:     hidden_group_size_z
      - .offset:         106
        .size:           2
        .value_kind:     hidden_remainder_x
      - .offset:         108
        .size:           2
        .value_kind:     hidden_remainder_y
      - .offset:         110
        .size:           2
        .value_kind:     hidden_remainder_z
      - .offset:         128
        .size:           8
        .value_kind:     hidden_global_offset_x
      - .offset:         136
        .size:           8
        .value_kind:     hidden_global_offset_y
      - .offset:         144
        .size:           8
        .value_kind:     hidden_global_offset_z
      - .offset:         152
        .size:           2
        .value_kind:     hidden_grid_dims
    .group_segment_fixed_size: 2048
    .kernarg_segment_align: 8
    .kernarg_segment_size: 344
    .language:       OpenCL C
    .language_version:
      - 2
      - 0
    .max_flat_workgroup_size: 256
    .name:           _Z7k_fold2PKfS0_S0_S0_S0_S0_S0_S0_S0_PDF16_Pf
    .private_segment_fixed_size: 0
    .sgpr_count:     36
    .sgpr_spill_count: 0
    .symbol:         _Z7k_fold2PKfS0_S0_S0_S0_S0_S0_S0_S0_PDF16_Pf.kd
    .uniform_work_group_size: 1
    .uses_dynamic_stack: false
    .vgpr_count:     61
    .vgpr_spill_count: 0
    .wavefront_size: 64
  - .agpr_count:     0
    .args:
      - .actual_access:  read_only
        .address_space:  global
        .offset:         0
        .size:           8
        .value_kind:     global_buffer
      - .actual_access:  read_only
        .address_space:  global
        .offset:         8
        .size:           8
        .value_kind:     global_buffer
      - .actual_access:  write_only
        .address_space:  global
        .offset:         16
        .size:           8
        .value_kind:     global_buffer
      - .actual_access:  read_only
        .address_space:  global
        .offset:         24
        .size:           8
        .value_kind:     global_buffer
      - .actual_access:  read_only
        .address_space:  global
        .offset:         32
        .size:           8
        .value_kind:     global_buffer
      - .actual_access:  read_only
        .address_space:  global
        .offset:         40
        .size:           8
        .value_kind:     global_buffer
      - .actual_access:  read_only
        .address_space:  global
        .offset:         48
        .size:           8
        .value_kind:     global_buffer
      - .actual_access:  read_only
        .address_space:  global
        .offset:         56
        .size:           8
        .value_kind:     global_buffer
      - .actual_access:  read_only
        .address_space:  global
        .offset:         64
        .size:           8
        .value_kind:     global_buffer
      - .actual_access:  read_only
        .address_space:  global
        .offset:         72
        .size:           8
        .value_kind:     global_buffer
      - .actual_access:  read_only
        .address_space:  global
        .offset:         80
        .size:           8
        .value_kind:     global_buffer
      - .actual_access:  write_only
        .address_space:  global
        .offset:         88
        .size:           8
        .value_kind:     global_buffer
      - .actual_access:  write_only
        .address_space:  global
        .offset:         96
        .size:           8
        .value_kind:     global_buffer
      - .address_space:  global
        .offset:         104
        .size:           8
        .value_kind:     global_buffer
      - .actual_access:  write_only
        .address_space:  global
        .offset:         112
        .size:           8
        .value_kind:     global_buffer
      - .actual_access:  read_only
        .address_space:  global
        .offset:         120
        .size:           8
        .value_kind:     global_buffer
      - .actual_access:  read_only
        .address_space:  global
        .offset:         128
        .size:           8
        .value_kind:     global_buffer
    .group_segment_fixed_size: 22272
    .kernarg_segment_align: 8
    .kernarg_segment_size: 136
    .language:       OpenCL C
    .language_version:
      - 2
      - 0
    .max_flat_workgroup_size: 256
    .name:           _Z5k_gcnILi1EEvPKvPK15HIP_vector_typeIiLj2EEPfPKiS8_PKfPKDF16_SA_SA_SA_SA_S6_PDF16_S6_SD_SC_SA_
    .private_segment_fixed_size: 0
    .sgpr_count:     35
    .sgpr_spill_count: 0
    .symbol:         _Z5k_gcnILi1EEvPKvPK15HIP_vector_typeIiLj2EEPfPKiS8_PKfPKDF16_SA_SA_SA_SA_S6_PDF16_S6_SD_SC_SA_.kd
    .uniform_work_group_size: 1
    .uses_dynamic_stack: false
    .vgpr_count:     58
    .vgpr_spill_count: 0
    .wavefront_size: 64
  - .agpr_count:     0
    .args:
      - .actual_access:  read_only
        .address_space:  global
        .offset:         0
        .size:           8
        .value_kind:     global_buffer
      - .actual_access:  read_only
        .address_space:  global
        .offset:         8
        .size:           8
        .value_kind:     global_buffer
      - .actual_access:  read_only
        .address_space:  global
        .offset:         16
        .size:           8
        .value_kind:     global_buffer
      - .actual_access:  read_only
        .address_space:  global
        .offset:         24
        .size:           8
        .value_kind:     global_buffer
      - .actual_access:  read_only
        .address_space:  global
        .offset:         32
        .size:           8
        .value_kind:     global_buffer
      - .actual_access:  read_only
        .address_space:  global
        .offset:         40
        .size:           8
        .value_kind:     global_buffer
      - .actual_access:  read_only
        .address_space:  global
        .offset:         48
        .size:           8
        .value_kind:     global_buffer
      - .actual_access:  read_only
        .address_space:  global
        .offset:         56
        .size:           8
        .value_kind:     global_buffer
      - .actual_access:  read_only
        .address_space:  global
        .offset:         64
        .size:           8
        .value_kind:     global_buffer
      - .actual_access:  read_only
        .address_space:  global
        .offset:         72
        .size:           8
        .value_kind:     global_buffer
      - .actual_access:  read_only
        .address_space:  global
        .offset:         80
        .size:           8
        .value_kind:     global_buffer
      - .actual_access:  read_only
        .address_space:  global
        .offset:         88
        .size:           8
        .value_kind:     global_buffer
      - .actual_access:  write_only
        .address_space:  global
        .offset:         96
        .size:           8
        .value_kind:     global_buffer
      - .address_space:  global
        .offset:         104
        .size:           8
        .value_kind:     global_buffer
      - .actual_access:  read_only
        .address_space:  global
        .offset:         112
        .size:           8
        .value_kind:     global_buffer
      - .actual_access:  read_only
        .address_space:  global
        .offset:         120
        .size:           8
        .value_kind:     global_buffer
      - .actual_access:  read_only
        .address_space:  global
        .offset:         128
        .size:           8
        .value_kind:     global_buffer
      - .offset:         136
        .size:           4
        .value_kind:     hidden_block_count_x
      - .offset:         140
        .size:           4
        .value_kind:     hidden_block_count_y
      - .offset:         144
        .size:           4
        .value_kind:     hidden_block_count_z
      - .offset:         148
        .size:           2
        .value_kind:     hidden_group_size_x
      - .offset:         150
        .size:           2
        .value_kind:     hidden_group_size_y
      - .offset:         152
        .size:           2
        .value_kind:     hidden_group_size_z
      - .offset:         154
        .size:           2
        .value_kind:     hidden_remainder_x
      - .offset:         156
        .size:           2
        .value_kind:     hidden_remainder_y
      - .offset:         158
        .size:           2
        .value_kind:     hidden_remainder_z
      - .offset:         176
        .size:           8
        .value_kind:     hidden_global_offset_x
      - .offset:         184
        .size:           8
        .value_kind:     hidden_global_offset_y
      - .offset:         192
        .size:           8
        .value_kind:     hidden_global_offset_z
      - .offset:         200
        .size:           2
        .value_kind:     hidden_grid_dims
    .group_segment_fixed_size: 23808
    .kernarg_segment_align: 8
    .kernarg_segment_size: 392
    .language:       OpenCL C
    .language_version:
      - 2
      - 0
    .max_flat_workgroup_size: 256
    .name:           _Z5k_gcnILi2EEvPKvPK15HIP_vector_typeIiLj2EEPfPKiS8_PKfPKDF16_SA_SA_SA_SA_S6_PDF16_S6_SD_SC_SA_
    .private_segment_fixed_size: 0
    .sgpr_count:     36
    .sgpr_spill_count: 0
    .symbol:         _Z5k_gcnILi2EEvPKvPK15HIP_vector_typeIiLj2EEPfPKiS8_PKfPKDF16_SA_SA_SA_SA_S6_PDF16_S6_SD_SC_SA_.kd
    .uniform_work_group_size: 1
    .uses_dynamic_stack: false
    .vgpr_count:     128
    .vgpr_spill_count: 0
    .wavefront_size: 64
  - .agpr_count:     0
    .args:
      - .actual_access:  read_only
        .address_space:  global
        .offset:         0
        .size:           8
        .value_kind:     global_buffer
      - .actual_access:  read_only
        .address_space:  global
        .offset:         8
        .size:           8
        .value_kind:     global_buffer
      - .actual_access:  read_only
        .address_space:  global
        .offset:         16
        .size:           8
        .value_kind:     global_buffer
      - .actual_access:  read_only
        .address_space:  global
        .offset:         24
        .size:           8
        .value_kind:     global_buffer
      - .actual_access:  write_only
        .address_space:  global
        .offset:         32
        .size:           8
        .value_kind:     global_buffer
      - .actual_access:  read_only
        .address_space:  global
        .offset:         40
        .size:           8
        .value_kind:     global_buffer
      - .actual_access:  read_only
        .address_space:  global
        .offset:         48
        .size:           8
        .value_kind:     global_buffer
      - .actual_access:  read_only
        .address_space:  global
        .offset:         56
        .size:           8
        .value_kind:     global_buffer
      - .actual_access:  read_only
        .address_space:  global
        .offset:         64
        .size:           8
        .value_kind:     global_buffer
      - .actual_access:  read_only
        .address_space:  global
        .offset:         72
        .size:           8
        .value_kind:     global_buffer
      - .actual_access:  read_only
        .address_space:  global
        .offset:         80
        .size:           8
        .value_kind:     global_buffer
      - .actual_access:  read_only
        .address_space:  global
        .offset:         88
        .size:           8
        .value_kind:     global_buffer
      - .actual_access:  write_only
        .address_space:  global
        .offset:         96
        .size:           8
        .value_kind:     global_buffer
    .group_segment_fixed_size: 9216
    .kernarg_segment_align: 8
    .kernarg_segment_size: 104
    .language:       OpenCL C
    .language_version:
      - 2
      - 0
    .max_flat_workgroup_size: 512
    .name:           _Z6k_lstmILi256ELi10ELb1ELb0EEvPKDF16_S1_S1_PKfPDF16_S1_S1_S1_S3_S3_S3_PfS5_
    .private_segment_fixed_size: 0
    .sgpr_count:     37
    .sgpr_spill_count: 0
    .symbol:         _Z6k_lstmILi256ELi10ELb1ELb0EEvPKDF16_S1_S1_PKfPDF16_S1_S1_S1_S3_S3_S3_PfS5_.kd
    .uniform_work_group_size: 1
    .uses_dynamic_stack: false
    .vgpr_count:     256
    .vgpr_spill_count: 0
    .wavefront_size: 64
  - .agpr_count:     0
    .args:
      - .actual_access:  read_only
        .address_space:  global
        .offset:         0
        .size:           8
        .value_kind:     global_buffer
      - .actual_access:  read_only
        .address_space:  global
        .offset:         8
        .size:           8
        .value_kind:     global_buffer
      - .actual_access:  read_only
        .address_space:  global
        .offset:         16
        .size:           8
        .value_kind:     global_buffer
      - .actual_access:  read_only
        .address_space:  global
        .offset:         24
        .size:           8
        .value_kind:     global_buffer
      - .actual_access:  read_only
        .address_space:  global
        .offset:         32
        .size:           8
        .value_kind:     global_buffer
      - .actual_access:  read_only
        .address_space:  global
        .offset:         40
        .size:           8
        .value_kind:     global_buffer
      - .actual_access:  read_only
        .address_space:  global
        .offset:         48
        .size:           8
        .value_kind:     global_buffer
      - .actual_access:  read_only
        .address_space:  global
        .offset:         56
        .size:           8
        .value_kind:     global_buffer
      - .actual_access:  read_only
        .address_space:  global
        .offset:         64
        .size:           8
        .value_kind:     global_buffer
      - .actual_access:  read_only
        .address_space:  global
        .offset:         72
        .size:           8
        .value_kind:     global_buffer
      - .actual_access:  read_only
        .address_space:  global
        .offset:         80
        .size:           8
        .value_kind:     global_buffer
      - .actual_access:  write_only
        .address_space:  global
        .offset:         88
        .size:           8
        .value_kind:     global_buffer
      - .actual_access:  read_only
        .address_space:  global
        .offset:         96
        .size:           8
        .value_kind:     global_buffer
    .group_segment_fixed_size: 0
    .kernarg_segment_align: 8
    .kernarg_segment_size: 104
    .language:       OpenCL C
    .language_version:
      - 2
      - 0
    .max_flat_workgroup_size: 512
    .name:           _Z6k_lstmILi128ELi8ELb0ELb1EEvPKDF16_S1_S1_PKfPDF16_S1_S1_S1_S3_S3_S3_PfS5_
    .private_segment_fixed_size: 0
    .sgpr_count:     46
    .sgpr_spill_count: 0
    .symbol:         _Z6k_lstmILi128ELi8ELb0ELb1EEvPKDF16_S1_S1_PKfPDF16_S1_S1_S1_S3_S3_S3_PfS5_.kd
    .uniform_work_group_size: 1
    .uses_dynamic_stack: false
    .vgpr_count:     256
    .vgpr_spill_count: 0
    .wavefront_size: 64
